# grid barrier: all workgroups poll the top generation word directly (no per-XCD relay hop, XCD-last no longer bumps the relay)
# speedup vs baseline: 1.0207x; 1.0042x over previous
.LBB0_295:
	s_or_b64 exec, exec, s[6:7]
	v_cvt_f32_u32_e32 v5, v3
	s_waitcnt vmcnt(0)
	v_readfirstlane_b32 s6, v4
	v_sub_u32_e32 v4, 0, v3
	v_rcp_iflag_f32_e32 v5, v5
	v_add_u32_e32 v6, s6, v0
	v_mul_f32_e32 v5, 0x4f7ffffe, v5
	v_cvt_u32_f32_e32 v5, v5
	v_mul_lo_u32 v0, v4, v5
	v_mul_hi_u32 v0, v5, v0
	v_add_u32_e32 v0, v5, v0
	v_mul_hi_u32 v0, v6, v0
	v_mul_lo_u32 v4, v0, v3
	v_sub_u32_e32 v4, v6, v4
	v_add_u32_e32 v5, 1, v0
	v_cmp_ge_u32_e32 vcc, v4, v3
	s_nop 1
	v_cndmask_b32_e32 v0, v0, v5, vcc
	v_sub_u32_e32 v5, v4, v3
	v_cndmask_b32_e32 v4, v4, v5, vcc
	v_add_u32_e32 v5, 1, v0
	v_cmp_ge_u32_e32 vcc, v4, v3
	v_add_u32_e32 v4, 1, v6
	s_nop 0
	v_cndmask_b32_e32 v0, v0, v5, vcc
	v_mul_lo_u32 v5, v3, v0
	v_add_u32_e32 v3, v5, v3
	v_cmp_ne_u32_e32 vcc, v4, v3
	s_and_saveexec_b64 s[6:7], vcc
	s_xor_b64 s[6:7], exec, s[6:7]
	s_cbranch_execz .LBB0_309
	v_readlane_b32 s8, v254, 9
	v_readlane_b32 s9, v254, 10
	s_waitcnt lgkmcnt(0)
	s_nop 3
	global_load_dword v2, v1, s[8:9] sc1
	s_waitcnt vmcnt(0)
	v_cmp_eq_u32_e32 vcc, v2, v0
	s_and_saveexec_b64 s[8:9], vcc
	s_cbranch_execz .LBB0_308
	s_mov_b32 s24, 1
	s_mov_b64 s[10:11], 0
	s_branch .LBB0_299

.LBB0_326:
	s_or_b64 exec, exec, s[6:7]
	s_mov_b64 s[6:7], exec
	v_mbcnt_lo_u32_b32 v0, s6, 0
	v_mbcnt_hi_u32_b32 v0, s7, v0
	v_cmp_eq_u32_e32 vcc, 0, v0
	s_waitcnt vmcnt(0)
	buffer_inv sc1
	s_and_saveexec_b64 s[8:9], vcc
	s_cbranch_execz .LBB0_328
	s_bcnt1_i32_b64 s6, s[6:7]
	v_mov_b32_e32 v0, s6
	v_readlane_b32 s6, v254, 5
	v_readlane_b32 s7, v254, 6
	s_nop 4
.LBB0_328:
	s_or_b64 exec, exec, s[8:9]
	s_waitcnt vmcnt(0)

.LBB0_421:
	s_or_b64 exec, exec, s[6:7]
	s_mov_b64 s[6:7], exec
	v_mbcnt_lo_u32_b32 v0, s6, 0
	v_mbcnt_hi_u32_b32 v0, s7, v0
	v_cmp_eq_u32_e32 vcc, 0, v0
	s_waitcnt vmcnt(0)
	buffer_inv sc1
	s_and_saveexec_b64 s[8:9], vcc
	s_cbranch_execz .LBB0_423
	s_bcnt1_i32_b64 s6, s[6:7]
	v_mov_b32_e32 v0, s6
	v_readlane_b32 s6, v254, 5
	v_readlane_b32 s7, v254, 6
	s_nop 4
.LBB0_423:
	s_or_b64 exec, exec, s[8:9]
	s_waitcnt vmcnt(0)

.LBB0_804:
	s_or_b64 exec, exec, s[6:7]
	s_mov_b64 s[6:7], exec
	v_mbcnt_lo_u32_b32 v0, s6, 0
	v_mbcnt_hi_u32_b32 v0, s7, v0
	v_cmp_eq_u32_e32 vcc, 0, v0
	s_waitcnt vmcnt(0)
	buffer_inv sc1
	s_and_saveexec_b64 s[8:9], vcc
	s_cbranch_execz .LBB0_806
	s_bcnt1_i32_b64 s6, s[6:7]
	v_mov_b32_e32 v0, s6
	v_readlane_b32 s6, v254, 5
	v_readlane_b32 s7, v254, 6
	s_nop 4
.LBB0_806:
	s_or_b64 exec, exec, s[8:9]
	s_waitcnt vmcnt(0)

.LBB0_919:
	s_or_b64 exec, exec, s[6:7]
	s_mov_b64 s[6:7], exec
	v_mbcnt_lo_u32_b32 v0, s6, 0
	v_mbcnt_hi_u32_b32 v0, s7, v0
	v_cmp_eq_u32_e32 vcc, 0, v0
	s_waitcnt vmcnt(0)
	buffer_inv sc1
	s_and_saveexec_b64 s[8:9], vcc
	s_cbranch_execz .LBB0_921
	s_bcnt1_i32_b64 s6, s[6:7]
	v_mov_b32_e32 v0, s6
	v_readlane_b32 s6, v254, 5
	v_readlane_b32 s7, v254, 6
	s_nop 4
.LBB0_921:
	s_or_b64 exec, exec, s[8:9]
	s_waitcnt vmcnt(0)

.LBB0_1132:
	s_or_b64 exec, exec, s[6:7]
	s_mov_b64 s[6:7], exec
	v_mbcnt_lo_u32_b32 v0, s6, 0
	v_mbcnt_hi_u32_b32 v0, s7, v0
	v_cmp_eq_u32_e32 vcc, 0, v0
	s_waitcnt vmcnt(0)
	buffer_inv sc1
	s_and_saveexec_b64 s[8:9], vcc
	s_cbranch_execz .LBB0_1134
	s_bcnt1_i32_b64 s6, s[6:7]
	v_mov_b32_e32 v0, s6
	v_readlane_b32 s6, v254, 5
	v_readlane_b32 s7, v254, 6
	s_nop 4
.LBB0_1134:
	s_or_b64 exec, exec, s[8:9]
	s_waitcnt vmcnt(0)

.LBB0_1193:
	s_or_b64 exec, exec, s[6:7]
	s_mov_b64 s[6:7], exec
	v_mbcnt_lo_u32_b32 v0, s6, 0
	v_mbcnt_hi_u32_b32 v0, s7, v0
	v_cmp_eq_u32_e32 vcc, 0, v0
	s_waitcnt vmcnt(0)
	buffer_inv sc1
	s_and_saveexec_b64 s[8:9], vcc
	s_cbranch_execz .LBB0_1195
	s_bcnt1_i32_b64 s6, s[6:7]
	v_mov_b32_e32 v0, s6
	v_readlane_b32 s6, v254, 5
	v_readlane_b32 s7, v254, 6
	s_nop 4
.LBB0_1195:
	s_or_b64 exec, exec, s[8:9]
	s_waitcnt vmcnt(0)

.LBB0_1282:
	s_or_b64 exec, exec, s[6:7]
	s_mov_b64 s[6:7], exec
	v_mbcnt_lo_u32_b32 v0, s6, 0
	v_mbcnt_hi_u32_b32 v0, s7, v0
	v_cmp_eq_u32_e32 vcc, 0, v0
	s_waitcnt vmcnt(0)
	buffer_inv sc1
	s_and_saveexec_b64 s[8:9], vcc
	s_cbranch_execz .LBB0_1284
	s_bcnt1_i32_b64 s6, s[6:7]
	v_mov_b32_e32 v0, s6
	v_readlane_b32 s6, v254, 5
	v_readlane_b32 s7, v254, 6
	s_nop 4
.LBB0_1284:
	s_or_b64 exec, exec, s[8:9]
	s_waitcnt vmcnt(0)

.LBB0_1428:
	s_or_b64 exec, exec, s[6:7]
	s_mov_b64 s[6:7], exec
	v_mbcnt_lo_u32_b32 v0, s6, 0
	v_mbcnt_hi_u32_b32 v0, s7, v0
	v_cmp_eq_u32_e32 vcc, 0, v0
	s_waitcnt vmcnt(0)
	buffer_inv sc1
	s_and_saveexec_b64 s[8:9], vcc
	s_cbranch_execz .LBB0_1430
	s_bcnt1_i32_b64 s6, s[6:7]
	v_mov_b32_e32 v0, s6
	v_readlane_b32 s6, v254, 5
	v_readlane_b32 s7, v254, 6
	s_nop 4
.LBB0_1430:
	s_or_b64 exec, exec, s[8:9]
	s_waitcnt vmcnt(0)

.LBB0_1525:
	s_or_b64 exec, exec, s[6:7]
	s_mov_b64 s[6:7], exec
	v_mbcnt_lo_u32_b32 v0, s6, 0
	v_mbcnt_hi_u32_b32 v0, s7, v0
	v_cmp_eq_u32_e32 vcc, 0, v0
	s_waitcnt vmcnt(0)
	buffer_inv sc1
	s_and_saveexec_b64 s[8:9], vcc
	s_cbranch_execz .LBB0_1527
	s_bcnt1_i32_b64 s6, s[6:7]
	v_mov_b32_e32 v0, s6
	v_readlane_b32 s6, v254, 5
	v_readlane_b32 s7, v254, 6
	s_nop 4
.LBB0_1527:
	s_or_b64 exec, exec, s[8:9]
	s_waitcnt vmcnt(0)

.LBB0_1573:
	s_or_b64 exec, exec, s[6:7]
	v_cvt_f32_u32_e32 v5, v3
	s_waitcnt vmcnt(0)
	v_readfirstlane_b32 s6, v4
	v_sub_u32_e32 v4, 0, v3
	v_rcp_iflag_f32_e32 v5, v5
	v_add_u32_e32 v6, s6, v0
	v_mul_f32_e32 v5, 0x4f7ffffe, v5
	v_cvt_u32_f32_e32 v5, v5
	v_mul_lo_u32 v0, v4, v5
	v_mul_hi_u32 v0, v5, v0
	v_add_u32_e32 v0, v5, v0
	v_mul_hi_u32 v0, v6, v0
	v_mul_lo_u32 v4, v0, v3
	v_sub_u32_e32 v4, v6, v4
	v_add_u32_e32 v5, 1, v0
	v_cmp_ge_u32_e32 vcc, v4, v3
	s_nop 1
	v_cndmask_b32_e32 v0, v0, v5, vcc
	v_sub_u32_e32 v5, v4, v3
	v_cndmask_b32_e32 v4, v4, v5, vcc
	v_add_u32_e32 v5, 1, v0
	v_cmp_ge_u32_e32 vcc, v4, v3
	v_add_u32_e32 v4, 1, v6
	s_nop 0
	v_cndmask_b32_e32 v0, v0, v5, vcc
	v_mul_lo_u32 v5, v3, v0
	v_add_u32_e32 v3, v5, v3
	v_cmp_ne_u32_e32 vcc, v4, v3
	s_and_saveexec_b64 s[6:7], vcc
	s_xor_b64 s[6:7], exec, s[6:7]
	s_cbranch_execz .LBB0_1587
	v_readlane_b32 s8, v254, 9
	v_readlane_b32 s9, v254, 10
	s_waitcnt lgkmcnt(0)
	s_nop 3
	global_load_dword v2, v1, s[8:9] sc1
	s_waitcnt vmcnt(0)
	v_cmp_eq_u32_e32 vcc, v2, v0
	s_and_saveexec_b64 s[8:9], vcc
	s_cbranch_execz .LBB0_1586
	s_mov_b32 s20, 1
	s_mov_b64 s[10:11], 0
	s_branch .LBB0_1577

.LBB0_1605:
	s_bcnt1_i32_b64 s6, s[6:7]
	v_mov_b32_e32 v0, s6
	v_readlane_b32 s6, v254, 5
	v_readlane_b32 s7, v254, 6
	s_nop 4
	s_getpc_b64 s[98:99]
